# v50 plus the 7 per-tile token-mask ballots of a sel-attn round computed by one lane-parallel lookup before the round barrier
# speedup vs baseline: 1.0110x; 1.0076x over previous
; #define LAS __attribute__((address_space(3)))
;     ...
;               for (int ts = 0; ts < TS; ++ts) {
;                 const int p0 = p0s[ts]; const int LK = AT_K + ts * AT_TS, LV = AT_V + ts * AT_TS;
;                 if (p0 < 0) continue;
;                 if (MODE == 0) { if (p0 > tw0 + TW - 1 || p0 + 63 < tw0 - 127) continue; }
;                 if (MODE == 1) { if (p0 > tw0 + TW - 1 || p0 + 63 < tw0 - 511) continue; }
;                 if (MODE == 2) { if (16 * p0 + 31 > tw0 + TW - 1) continue; }
;                 if (MODE == 3) { if (p0 > tw0 + TW - 1) continue; }
;                 const bool far = (MODE == 2) ? (tw0 - (16 * (p0 + 63) + 31) >= 790) : ((MODE == 3) ? (tw0 - (p0 + 63) >= 790) : false);
;                 const int jblk = p0 >> 6;
;                 bf16x8 akf[4][2]; bf16x8 avf[2][4];
;                 if (MODE != 3) {
; #pragma unroll
;                     for (int kt = 0; kt < 4; ++kt)
; #pragma unroll
;                         for (int ks = 0; ks < 2; ++ks) akf[kt][ks] = *(const LAS bf16x8*)(L + LK + (16 * kt + n) * 128 + ((((4 * ks + q) ^ n) & 7) << 4));
;                     if (do_pv) {
; #pragma unroll
;                         for (int st = 0; st < 2; ++st)
; #pragma unroll
;                             for (int dt = 0; dt < 4; ++dt) avf[st][dt] = *(const LAS bf16x8*)(L + LV + (16 * dt + n) * 128 + ((((4 * st + q) ^ n) & 7) << 4)); }
;                 }
;                 unsigned tokmask = 0u;
;                 if (MODE == 3) { tokmask = (unsigned)__ballot(lane < TW && ((selm[(wave * TW + (lane & (TW - 1))) * 8 + (jblk >> 5)] >> (jblk & 31)) & 1u)); if (tokmask == 0u) continue; }
.LBB0_1153:
	v_mbcnt_lo_u32_b32 v106, -1, 0
	v_mbcnt_hi_u32_b32 v106, -1, v106
	s_add_i32 s0, s55, -13
	v_lshrrev_b32_e32 v107, 3, v106
	v_add_u32_e32 v107, s0, v107
	s_add_i32 s0, 0, 0x25080
	v_min_i32_e32 v107, s52, v107
	v_lshl_add_u32 v107, v107, 2, s0
	ds_read_b32 v107, v107
	s_waitcnt lgkmcnt(0)
	v_lshrrev_b32_e32 v106, 5, v107
	v_lshl_add_u32 v106, v106, 2, v157
	ds_read_b32 v106, v106
	s_waitcnt lgkmcnt(0)
	v_lshrrev_b32_e32 v106, v107, v106
	v_and_b32_e32 v106, 1, v106
	v_cmp_eq_u32_e64 s[90:91], 1, v106
	s_cmp_lt_i32 s67, 0
	s_cselect_b64 s[0:1], -1, 0
	s_cmp_gt_i32 s67, s15
	s_cselect_b64 s[2:3], -1, 0
	s_or_b64 s[0:1], s[0:1], s[2:3]
	s_and_b64 vcc, exec, s[0:1]
	s_waitcnt lgkmcnt(0)
	s_barrier
	s_cbranch_vccnz .LBB0_1175
	s_bfe_u32 s0, s90, 0x80000
	s_cmp_eq_u32 s0, 0
	s_cbranch_scc1 .LBB0_1175
	s_sub_i32 s1, s16, s67
	s_cmpk_lt_i32 s1, 0x316
	s_cselect_b64 s[2:3], -1, 0
	v_cndmask_b32_e64 v106, 0, 1, s[2:3]
	s_and_b32 s1, s0, 15
	s_cmp_eq_u32 s1, 0
	v_cmp_ne_u32_e64 s[2:3], 1, v106
	s_cbranch_scc1 .LBB0_1166
	v_add_u32_e32 v238, v187, v195
	v_add_u32_e32 v237, v187, v204
	ds_read_b128 v[106:109], v238
	ds_read_b128 v[110:113], v238 offset:2048
	ds_read_b128 v[126:129], v237
	ds_read_b128 v[114:117], v237 offset:2048
	ds_read_b128 v[118:121], v238 offset:4096
	ds_read_b128 v[122:125], v238 offset:6144
	ds_read_b128 v[134:137], v237 offset:4096
	ds_read_b128 v[130:133], v237 offset:6144
	s_and_b64 vcc, exec, s[2:3]
	s_cbranch_vccnz .LBB0_1160
	v_sub_u32_e32 v138, s67, v196
	v_lshl_add_u32 v138, v138, 2, v233
	v_add_u32_e32 v139, 0xffc, v138
	v_add_u32_e32 v140, 0x1004, v138
	v_add_u32_e32 v141, 0x103c, v138
	v_add_u32_e32 v142, 0x1044, v138
	ds_read2_b32 v[168:169], v139 offset1:1
	ds_read2_b32 v[170:171], v140 offset1:1
	ds_read2_b32 v[172:173], v141 offset1:1
	ds_read2_b32 v[174:175], v142 offset1:1
	v_add_u32_e32 v139, 0x107c, v138
	v_add_u32_e32 v140, 0x1084, v138
	v_add_u32_e32 v141, 0x10bc, v138
	v_add_u32_e32 v138, 0x10c4, v138
	ds_read2_b32 v[176:177], v139 offset1:1
	ds_read2_b32 v[178:179], v140 offset1:1
	ds_read2_b32 v[180:181], v141 offset1:1
	ds_read2_b32 v[182:183], v138 offset1:1

; #define LAS __attribute__((address_space(3)))
;     ...
;               for (int ts = 0; ts < TS; ++ts) {
;                 const int p0 = p0s[ts]; const int LK = AT_K + ts * AT_TS, LV = AT_V + ts * AT_TS;
;                 if (p0 < 0) continue;
;                 if (MODE == 0) { if (p0 > tw0 + TW - 1 || p0 + 63 < tw0 - 127) continue; }
;                 if (MODE == 1) { if (p0 > tw0 + TW - 1 || p0 + 63 < tw0 - 511) continue; }
;                 if (MODE == 2) { if (16 * p0 + 31 > tw0 + TW - 1) continue; }
;                 if (MODE == 3) { if (p0 > tw0 + TW - 1) continue; }
;                 const bool far = (MODE == 2) ? (tw0 - (16 * (p0 + 63) + 31) >= 790) : ((MODE == 3) ? (tw0 - (p0 + 63) >= 790) : false);
;                 const int jblk = p0 >> 6;
;                 bf16x8 akf[4][2]; bf16x8 avf[2][4];
;                 if (MODE != 3) {
; #pragma unroll
;                     for (int kt = 0; kt < 4; ++kt)
; #pragma unroll
;                         for (int ks = 0; ks < 2; ++ks) akf[kt][ks] = *(const LAS bf16x8*)(L + LK + (16 * kt + n) * 128 + ((((4 * ks + q) ^ n) & 7) << 4));
;                     if (do_pv) {
; #pragma unroll
;                         for (int st = 0; st < 2; ++st)
; #pragma unroll
;                             for (int dt = 0; dt < 4; ++dt) avf[st][dt] = *(const LAS bf16x8*)(L + LV + (16 * dt + n) * 128 + ((((4 * st + q) ^ n) & 7) << 4)); }
;                 }
;                 unsigned tokmask = 0u;
;                 if (MODE == 3) { tokmask = (unsigned)__ballot(lane < TW && ((selm[(wave * TW + (lane & (TW - 1))) * 8 + (jblk >> 5)] >> (jblk & 31)) & 1u)); if (tokmask == 0u) continue; }
.LBB0_1175:
	s_cmp_lt_i32 s66, 0
	s_cselect_b64 s[0:1], -1, 0
	s_cmp_gt_i32 s66, s15
	s_cselect_b64 s[2:3], -1, 0
	s_or_b64 s[0:1], s[0:1], s[2:3]
	s_and_b64 vcc, exec, s[0:1]
	s_cbranch_vccnz .LBB0_1197
	s_bfe_u32 s0, s90, 0x80008
	s_cmp_eq_u32 s0, 0
	s_cbranch_scc1 .LBB0_1197
	s_sub_i32 s1, s16, s66
	s_cmpk_lt_i32 s1, 0x316
	s_cselect_b64 s[2:3], -1, 0
	v_cndmask_b32_e64 v106, 0, 1, s[2:3]
	s_and_b32 s1, s0, 15
	s_cmp_eq_u32 s1, 0
	v_cmp_ne_u32_e64 s[2:3], 1, v106
	s_cbranch_scc1 .LBB0_1188
	v_add_u32_e32 v238, v187, v195
	v_add_u32_e32 v237, v187, v204
	ds_read_b128 v[106:109], v238 offset:16384
	ds_read_b128 v[110:113], v238 offset:18432
	ds_read_b128 v[126:129], v237 offset:16384
	ds_read_b128 v[114:117], v237 offset:18432
	ds_read_b128 v[118:121], v238 offset:20480
	ds_read_b128 v[122:125], v238 offset:22528
	ds_read_b128 v[134:137], v237 offset:20480
	ds_read_b128 v[130:133], v237 offset:22528
	s_and_b64 vcc, exec, s[2:3]
	s_cbranch_vccnz .LBB0_1182
	v_sub_u32_e32 v138, s66, v196
	v_lshl_add_u32 v138, v138, 2, v233
	v_add_u32_e32 v139, 0xffc, v138
	v_add_u32_e32 v140, 0x1004, v138
	v_add_u32_e32 v141, 0x103c, v138
	v_add_u32_e32 v142, 0x1044, v138
	ds_read2_b32 v[168:169], v139 offset1:1
	ds_read2_b32 v[170:171], v140 offset1:1
	ds_read2_b32 v[172:173], v141 offset1:1
	ds_read2_b32 v[174:175], v142 offset1:1
	v_add_u32_e32 v139, 0x107c, v138
	v_add_u32_e32 v140, 0x1084, v138
	v_add_u32_e32 v141, 0x10bc, v138
	v_add_u32_e32 v138, 0x10c4, v138
	ds_read2_b32 v[176:177], v139 offset1:1
	ds_read2_b32 v[178:179], v140 offset1:1
	ds_read2_b32 v[180:181], v141 offset1:1
	ds_read2_b32 v[182:183], v138 offset1:1

; #define LAS __attribute__((address_space(3)))
;     ...
;               for (int ts = 0; ts < TS; ++ts) {
;                 const int p0 = p0s[ts]; const int LK = AT_K + ts * AT_TS, LV = AT_V + ts * AT_TS;
;                 if (p0 < 0) continue;
;                 if (MODE == 0) { if (p0 > tw0 + TW - 1 || p0 + 63 < tw0 - 127) continue; }
;                 if (MODE == 1) { if (p0 > tw0 + TW - 1 || p0 + 63 < tw0 - 511) continue; }
;                 if (MODE == 2) { if (16 * p0 + 31 > tw0 + TW - 1) continue; }
;                 if (MODE == 3) { if (p0 > tw0 + TW - 1) continue; }
;                 const bool far = (MODE == 2) ? (tw0 - (16 * (p0 + 63) + 31) >= 790) : ((MODE == 3) ? (tw0 - (p0 + 63) >= 790) : false);
;                 const int jblk = p0 >> 6;
;                 bf16x8 akf[4][2]; bf16x8 avf[2][4];
;                 if (MODE != 3) {
; #pragma unroll
;                     for (int kt = 0; kt < 4; ++kt)
; #pragma unroll
;                         for (int ks = 0; ks < 2; ++ks) akf[kt][ks] = *(const LAS bf16x8*)(L + LK + (16 * kt + n) * 128 + ((((4 * ks + q) ^ n) & 7) << 4));
;                     if (do_pv) {
; #pragma unroll
;                         for (int st = 0; st < 2; ++st)
; #pragma unroll
;                             for (int dt = 0; dt < 4; ++dt) avf[st][dt] = *(const LAS bf16x8*)(L + LV + (16 * dt + n) * 128 + ((((4 * st + q) ^ n) & 7) << 4)); }
;                 }
;                 unsigned tokmask = 0u;
;                 if (MODE == 3) { tokmask = (unsigned)__ballot(lane < TW && ((selm[(wave * TW + (lane & (TW - 1))) * 8 + (jblk >> 5)] >> (jblk & 31)) & 1u)); if (tokmask == 0u) continue; }
.LBB0_1197:
	s_cmp_lt_i32 s65, 0
	s_cselect_b64 s[0:1], -1, 0
	s_cmp_gt_i32 s65, s15
	s_cselect_b64 s[2:3], -1, 0
	s_or_b64 s[0:1], s[0:1], s[2:3]
	s_and_b64 vcc, exec, s[0:1]
	s_cbranch_vccnz .LBB0_1219
	s_bfe_u32 s0, s90, 0x80010
	s_cmp_eq_u32 s0, 0
	s_cbranch_scc1 .LBB0_1219
	s_sub_i32 s1, s16, s65
	s_cmpk_lt_i32 s1, 0x316
	s_cselect_b64 s[2:3], -1, 0
	v_cndmask_b32_e64 v106, 0, 1, s[2:3]
	s_and_b32 s1, s0, 15
	s_cmp_eq_u32 s1, 0
	v_cmp_ne_u32_e64 s[2:3], 1, v106
	s_cbranch_scc1 .LBB0_1210
	v_add_u32_e32 v238, v187, v195
	v_add_u32_e32 v237, v187, v204
	ds_read_b128 v[106:109], v238 offset:32768
	ds_read_b128 v[110:113], v238 offset:34816
	ds_read_b128 v[126:129], v237 offset:32768
	ds_read_b128 v[114:117], v237 offset:34816
	ds_read_b128 v[118:121], v238 offset:36864
	ds_read_b128 v[122:125], v238 offset:38912
	ds_read_b128 v[134:137], v237 offset:36864
	ds_read_b128 v[130:133], v237 offset:38912
	s_and_b64 vcc, exec, s[2:3]
	s_cbranch_vccnz .LBB0_1204
	v_sub_u32_e32 v138, s65, v196
	v_lshl_add_u32 v138, v138, 2, v233
	v_add_u32_e32 v139, 0xffc, v138
	v_add_u32_e32 v140, 0x1004, v138
	v_add_u32_e32 v141, 0x103c, v138
	v_add_u32_e32 v142, 0x1044, v138
	ds_read2_b32 v[168:169], v139 offset1:1
	ds_read2_b32 v[170:171], v140 offset1:1
	ds_read2_b32 v[172:173], v141 offset1:1
	ds_read2_b32 v[174:175], v142 offset1:1
	v_add_u32_e32 v139, 0x107c, v138
	v_add_u32_e32 v140, 0x1084, v138
	v_add_u32_e32 v141, 0x10bc, v138
	v_add_u32_e32 v138, 0x10c4, v138
	ds_read2_b32 v[176:177], v139 offset1:1
	ds_read2_b32 v[178:179], v140 offset1:1
	ds_read2_b32 v[180:181], v141 offset1:1
	ds_read2_b32 v[182:183], v138 offset1:1

; #define LAS __attribute__((address_space(3)))
;     ...
;               for (int ts = 0; ts < TS; ++ts) {
;                 const int p0 = p0s[ts]; const int LK = AT_K + ts * AT_TS, LV = AT_V + ts * AT_TS;
;                 if (p0 < 0) continue;
;                 if (MODE == 0) { if (p0 > tw0 + TW - 1 || p0 + 63 < tw0 - 127) continue; }
;                 if (MODE == 1) { if (p0 > tw0 + TW - 1 || p0 + 63 < tw0 - 511) continue; }
;                 if (MODE == 2) { if (16 * p0 + 31 > tw0 + TW - 1) continue; }
;                 if (MODE == 3) { if (p0 > tw0 + TW - 1) continue; }
;                 const bool far = (MODE == 2) ? (tw0 - (16 * (p0 + 63) + 31) >= 790) : ((MODE == 3) ? (tw0 - (p0 + 63) >= 790) : false);
;                 const int jblk = p0 >> 6;
;                 bf16x8 akf[4][2]; bf16x8 avf[2][4];
;                 if (MODE != 3) {
; #pragma unroll
;                     for (int kt = 0; kt < 4; ++kt)
; #pragma unroll
;                         for (int ks = 0; ks < 2; ++ks) akf[kt][ks] = *(const LAS bf16x8*)(L + LK + (16 * kt + n) * 128 + ((((4 * ks + q) ^ n) & 7) << 4));
;                     if (do_pv) {
; #pragma unroll
;                         for (int st = 0; st < 2; ++st)
; #pragma unroll
;                             for (int dt = 0; dt < 4; ++dt) avf[st][dt] = *(const LAS bf16x8*)(L + LV + (16 * dt + n) * 128 + ((((4 * st + q) ^ n) & 7) << 4)); }
;                 }
;                 unsigned tokmask = 0u;
;                 if (MODE == 3) { tokmask = (unsigned)__ballot(lane < TW && ((selm[(wave * TW + (lane & (TW - 1))) * 8 + (jblk >> 5)] >> (jblk & 31)) & 1u)); if (tokmask == 0u) continue; }
.LBB0_1219:
	s_cmp_lt_i32 s64, 0
	s_cselect_b64 s[0:1], -1, 0
	s_cmp_gt_i32 s64, s15
	s_cselect_b64 s[2:3], -1, 0
	s_or_b64 s[0:1], s[0:1], s[2:3]
	s_and_b64 vcc, exec, s[0:1]
	s_cbranch_vccnz .LBB0_1241
	s_bfe_u32 s0, s90, 0x80018
	s_cmp_eq_u32 s0, 0
	s_cbranch_scc1 .LBB0_1241
	s_sub_i32 s1, s16, s64
	s_cmpk_lt_i32 s1, 0x316
	s_cselect_b64 s[2:3], -1, 0
	s_and_b32 s1, s0, 15
	v_cndmask_b32_e64 v106, 0, 1, s[2:3]
	s_cmp_eq_u32 s1, 0
	v_add_u32_e32 v238, v187, v195
	v_add_u32_e32 v237, v187, v204
	v_cmp_ne_u32_e64 s[2:3], 1, v106
	s_cbranch_scc1 .LBB0_1232
	ds_read_b128 v[106:109], v238 offset:49152
	ds_read_b128 v[110:113], v238 offset:51200
	ds_read_b128 v[126:129], v237 offset:49152
	ds_read_b128 v[114:117], v237 offset:51200
	ds_read_b128 v[118:121], v238 offset:53248
	ds_read_b128 v[122:125], v238 offset:55296
	ds_read_b128 v[134:137], v237 offset:53248
	ds_read_b128 v[130:133], v237 offset:55296
	s_and_b64 vcc, exec, s[2:3]
	s_cbranch_vccnz .LBB0_1226
	v_sub_u32_e32 v138, s64, v196
	v_lshl_add_u32 v138, v138, 2, v233
	v_add_u32_e32 v139, 0xffc, v138
	v_add_u32_e32 v140, 0x1004, v138
	v_add_u32_e32 v141, 0x103c, v138
	v_add_u32_e32 v142, 0x1044, v138
	ds_read2_b32 v[168:169], v139 offset1:1
	ds_read2_b32 v[170:171], v140 offset1:1
	ds_read2_b32 v[172:173], v141 offset1:1
	ds_read2_b32 v[174:175], v142 offset1:1
	v_add_u32_e32 v139, 0x107c, v138
	v_add_u32_e32 v140, 0x1084, v138
	v_add_u32_e32 v141, 0x10bc, v138
	v_add_u32_e32 v138, 0x10c4, v138
	ds_read2_b32 v[176:177], v139 offset1:1
	ds_read2_b32 v[178:179], v140 offset1:1
	ds_read2_b32 v[180:181], v141 offset1:1
	ds_read2_b32 v[182:183], v138 offset1:1

; #define LAS __attribute__((address_space(3)))
;     ...
;               for (int ts = 0; ts < TS; ++ts) {
;                 const int p0 = p0s[ts]; const int LK = AT_K + ts * AT_TS, LV = AT_V + ts * AT_TS;
;                 if (p0 < 0) continue;
;                 if (MODE == 0) { if (p0 > tw0 + TW - 1 || p0 + 63 < tw0 - 127) continue; }
;                 if (MODE == 1) { if (p0 > tw0 + TW - 1 || p0 + 63 < tw0 - 511) continue; }
;                 if (MODE == 2) { if (16 * p0 + 31 > tw0 + TW - 1) continue; }
;                 if (MODE == 3) { if (p0 > tw0 + TW - 1) continue; }
;                 const bool far = (MODE == 2) ? (tw0 - (16 * (p0 + 63) + 31) >= 790) : ((MODE == 3) ? (tw0 - (p0 + 63) >= 790) : false);
;                 const int jblk = p0 >> 6;
;                 bf16x8 akf[4][2]; bf16x8 avf[2][4];
;                 if (MODE != 3) {
; #pragma unroll
;                     for (int kt = 0; kt < 4; ++kt)
; #pragma unroll
;                         for (int ks = 0; ks < 2; ++ks) akf[kt][ks] = *(const LAS bf16x8*)(L + LK + (16 * kt + n) * 128 + ((((4 * ks + q) ^ n) & 7) << 4));
;                     if (do_pv) {
; #pragma unroll
;                         for (int st = 0; st < 2; ++st)
; #pragma unroll
;                             for (int dt = 0; dt < 4; ++dt) avf[st][dt] = *(const LAS bf16x8*)(L + LV + (16 * dt + n) * 128 + ((((4 * st + q) ^ n) & 7) << 4)); }
;                 }
;                 unsigned tokmask = 0u;
;                 if (MODE == 3) { tokmask = (unsigned)__ballot(lane < TW && ((selm[(wave * TW + (lane & (TW - 1))) * 8 + (jblk >> 5)] >> (jblk & 31)) & 1u)); if (tokmask == 0u) continue; }
.LBB0_1241:
	s_cmp_lt_i32 s63, 0
	s_cselect_b64 s[0:1], -1, 0
	s_cmp_gt_i32 s63, s15
	s_cselect_b64 s[2:3], -1, 0
	s_or_b64 s[0:1], s[0:1], s[2:3]
	s_and_b64 vcc, exec, s[0:1]
	s_cbranch_vccnz .LBB0_1263
	s_bfe_u32 s0, s91, 0x80000
	s_cmp_eq_u32 s0, 0
	s_cbranch_scc1 .LBB0_1263
	s_sub_i32 s1, s16, s63
	s_cmpk_lt_i32 s1, 0x316
	s_cselect_b64 s[2:3], -1, 0
	s_and_b32 s1, s0, 15
	v_cndmask_b32_e64 v106, 0, 1, s[2:3]
	s_cmp_eq_u32 s1, 0
	v_add_u32_e32 v237, v206, v195
	v_add_u32_e32 v238, v206, v204
	v_add_u32_e32 v239, v208, v195
	v_add_u32_e32 v240, v208, v204
	v_add_u32_e32 v241, v209, v195
	v_add_u32_e32 v245, v209, v204
	v_add_u32_e32 v246, v210, v195
	v_add_u32_e32 v247, v210, v204
	v_cmp_ne_u32_e64 s[2:3], 1, v106
	s_cbranch_scc1 .LBB0_1254
	ds_read_b128 v[106:109], v237
	ds_read_b128 v[110:113], v238
	ds_read_b128 v[114:117], v239
	ds_read_b128 v[118:121], v240
	ds_read_b128 v[122:125], v241
	ds_read_b128 v[126:129], v245
	ds_read_b128 v[130:133], v246
	ds_read_b128 v[134:137], v247
	s_and_b64 vcc, exec, s[2:3]
	s_cbranch_vccnz .LBB0_1248
	v_sub_u32_e32 v138, s63, v196
	v_lshl_add_u32 v138, v138, 2, v233
	v_add_u32_e32 v139, 0xffc, v138
	v_add_u32_e32 v140, 0x1004, v138
	v_add_u32_e32 v141, 0x103c, v138
	v_add_u32_e32 v142, 0x1044, v138
	ds_read2_b32 v[168:169], v139 offset1:1
	ds_read2_b32 v[170:171], v140 offset1:1
	ds_read2_b32 v[172:173], v141 offset1:1
	ds_read2_b32 v[174:175], v142 offset1:1
	v_add_u32_e32 v139, 0x107c, v138
	v_add_u32_e32 v140, 0x1084, v138
	v_add_u32_e32 v141, 0x10bc, v138
	v_add_u32_e32 v138, 0x10c4, v138
	ds_read2_b32 v[176:177], v139 offset1:1
	ds_read2_b32 v[178:179], v140 offset1:1
	ds_read2_b32 v[180:181], v141 offset1:1
	ds_read2_b32 v[182:183], v138 offset1:1

; #define LAS __attribute__((address_space(3)))
;     ...
;               for (int ts = 0; ts < TS; ++ts) {
;                 const int p0 = p0s[ts]; const int LK = AT_K + ts * AT_TS, LV = AT_V + ts * AT_TS;
;                 if (p0 < 0) continue;
;                 if (MODE == 0) { if (p0 > tw0 + TW - 1 || p0 + 63 < tw0 - 127) continue; }
;                 if (MODE == 1) { if (p0 > tw0 + TW - 1 || p0 + 63 < tw0 - 511) continue; }
;                 if (MODE == 2) { if (16 * p0 + 31 > tw0 + TW - 1) continue; }
;                 if (MODE == 3) { if (p0 > tw0 + TW - 1) continue; }
;                 const bool far = (MODE == 2) ? (tw0 - (16 * (p0 + 63) + 31) >= 790) : ((MODE == 3) ? (tw0 - (p0 + 63) >= 790) : false);
;                 const int jblk = p0 >> 6;
;                 bf16x8 akf[4][2]; bf16x8 avf[2][4];
;                 if (MODE != 3) {
; #pragma unroll
;                     for (int kt = 0; kt < 4; ++kt)
; #pragma unroll
;                         for (int ks = 0; ks < 2; ++ks) akf[kt][ks] = *(const LAS bf16x8*)(L + LK + (16 * kt + n) * 128 + ((((4 * ks + q) ^ n) & 7) << 4));
;                     if (do_pv) {
; #pragma unroll
;                         for (int st = 0; st < 2; ++st)
; #pragma unroll
;                             for (int dt = 0; dt < 4; ++dt) avf[st][dt] = *(const LAS bf16x8*)(L + LV + (16 * dt + n) * 128 + ((((4 * st + q) ^ n) & 7) << 4)); }
;                 }
;                 unsigned tokmask = 0u;
;                 if (MODE == 3) { tokmask = (unsigned)__ballot(lane < TW && ((selm[(wave * TW + (lane & (TW - 1))) * 8 + (jblk >> 5)] >> (jblk & 31)) & 1u)); if (tokmask == 0u) continue; }
.LBB0_1263:
	s_cmp_lt_i32 s53, 0
	s_cselect_b64 s[0:1], -1, 0
	s_cmp_gt_i32 s53, s15
	s_cselect_b64 s[2:3], -1, 0
	s_or_b64 s[0:1], s[0:1], s[2:3]
	s_and_b64 vcc, exec, s[0:1]
	s_cbranch_vccnz .LBB0_1285
	s_bfe_u32 s0, s91, 0x80008
	s_cmp_eq_u32 s0, 0
	s_cbranch_scc1 .LBB0_1285
	s_sub_i32 s1, s16, s53
	s_cmpk_lt_i32 s1, 0x316
	s_cselect_b64 s[2:3], -1, 0
	s_and_b32 s1, s0, 15
	v_cndmask_b32_e64 v106, 0, 1, s[2:3]
	s_cmp_eq_u32 s1, 0
	v_add_u32_e32 v237, v211, v195
	v_add_u32_e32 v238, v211, v204
	v_add_u32_e32 v239, v213, v195
	v_add_u32_e32 v240, v213, v204
	v_add_u32_e32 v241, v214, v195
	v_add_u32_e32 v245, v214, v204
	v_add_u32_e32 v246, v215, v195
	v_add_u32_e32 v247, v215, v204
	v_cmp_ne_u32_e64 s[2:3], 1, v106
	s_cbranch_scc1 .LBB0_1276
	ds_read_b128 v[106:109], v237
	ds_read_b128 v[110:113], v238
	ds_read_b128 v[114:117], v239
	ds_read_b128 v[118:121], v240
	ds_read_b128 v[122:125], v241
	ds_read_b128 v[126:129], v245
	ds_read_b128 v[130:133], v246
	ds_read_b128 v[134:137], v247
	s_and_b64 vcc, exec, s[2:3]
	s_cbranch_vccnz .LBB0_1270
	v_sub_u32_e32 v138, s53, v196
	v_lshl_add_u32 v138, v138, 2, v233
	v_add_u32_e32 v139, 0xffc, v138
	v_add_u32_e32 v140, 0x1004, v138
	v_add_u32_e32 v141, 0x103c, v138
	v_add_u32_e32 v142, 0x1044, v138
	ds_read2_b32 v[168:169], v139 offset1:1
	ds_read2_b32 v[170:171], v140 offset1:1
	ds_read2_b32 v[172:173], v141 offset1:1
	ds_read2_b32 v[174:175], v142 offset1:1
	v_add_u32_e32 v139, 0x107c, v138
	v_add_u32_e32 v140, 0x1084, v138
	v_add_u32_e32 v141, 0x10bc, v138
	v_add_u32_e32 v138, 0x10c4, v138
	ds_read2_b32 v[176:177], v139 offset1:1
	ds_read2_b32 v[178:179], v140 offset1:1
	ds_read2_b32 v[180:181], v141 offset1:1
	ds_read2_b32 v[182:183], v138 offset1:1

; #define LAS __attribute__((address_space(3)))
;     ...
;               for (int ts = 0; ts < TS; ++ts) {
;                 const int p0 = p0s[ts]; const int LK = AT_K + ts * AT_TS, LV = AT_V + ts * AT_TS;
;                 if (p0 < 0) continue;
;                 if (MODE == 0) { if (p0 > tw0 + TW - 1 || p0 + 63 < tw0 - 127) continue; }
;                 if (MODE == 1) { if (p0 > tw0 + TW - 1 || p0 + 63 < tw0 - 511) continue; }
;                 if (MODE == 2) { if (16 * p0 + 31 > tw0 + TW - 1) continue; }
;                 if (MODE == 3) { if (p0 > tw0 + TW - 1) continue; }
;                 const bool far = (MODE == 2) ? (tw0 - (16 * (p0 + 63) + 31) >= 790) : ((MODE == 3) ? (tw0 - (p0 + 63) >= 790) : false);
;                 const int jblk = p0 >> 6;
;                 bf16x8 akf[4][2]; bf16x8 avf[2][4];
;                 if (MODE != 3) {
; #pragma unroll
;                     for (int kt = 0; kt < 4; ++kt)
; #pragma unroll
;                         for (int ks = 0; ks < 2; ++ks) akf[kt][ks] = *(const LAS bf16x8*)(L + LK + (16 * kt + n) * 128 + ((((4 * ks + q) ^ n) & 7) << 4));
;                     if (do_pv) {
; #pragma unroll
;                         for (int st = 0; st < 2; ++st)
; #pragma unroll
;                             for (int dt = 0; dt < 4; ++dt) avf[st][dt] = *(const LAS bf16x8*)(L + LV + (16 * dt + n) * 128 + ((((4 * st + q) ^ n) & 7) << 4)); }
;                 }
;                 unsigned tokmask = 0u;
;                 if (MODE == 3) { tokmask = (unsigned)__ballot(lane < TW && ((selm[(wave * TW + (lane & (TW - 1))) * 8 + (jblk >> 5)] >> (jblk & 31)) & 1u)); if (tokmask == 0u) continue; }
.LBB0_1285:
	s_cmp_lt_i32 s29, 0
	s_cselect_b64 s[0:1], -1, 0
	s_cmp_gt_i32 s29, s15
	s_cselect_b64 s[2:3], -1, 0
	s_or_b64 s[0:1], s[0:1], s[2:3]
	s_and_b64 vcc, exec, s[0:1]
	s_cbranch_vccnz .LBB0_1307
	s_bfe_u32 s0, s91, 0x80010
	s_cmp_eq_u32 s0, 0
	s_cbranch_scc1 .LBB0_1307
	s_sub_i32 s1, s16, s29
	s_cmpk_lt_i32 s1, 0x316
	s_cselect_b64 s[2:3], -1, 0
	s_and_b32 s1, s0, 15
	v_cndmask_b32_e64 v106, 0, 1, s[2:3]
	s_cmp_eq_u32 s1, 0
	v_add_u32_e32 v237, v216, v195
	v_add_u32_e32 v238, v216, v204
	v_add_u32_e32 v239, v218, v195
	v_add_u32_e32 v240, v218, v204
	v_add_u32_e32 v241, v219, v195
	v_add_u32_e32 v245, v219, v204
	v_add_u32_e32 v246, v220, v195
	v_add_u32_e32 v247, v220, v204
	v_cmp_ne_u32_e64 s[2:3], 1, v106
	s_cbranch_scc1 .LBB0_1298
	ds_read_b128 v[106:109], v237
	ds_read_b128 v[110:113], v238
	ds_read_b128 v[114:117], v239
	ds_read_b128 v[118:121], v240
	ds_read_b128 v[122:125], v241
	ds_read_b128 v[126:129], v245
	ds_read_b128 v[130:133], v246
	ds_read_b128 v[134:137], v247
	s_and_b64 vcc, exec, s[2:3]
	s_cbranch_vccnz .LBB0_1292
	v_sub_u32_e32 v138, s29, v196
	v_lshl_add_u32 v138, v138, 2, v233
	v_add_u32_e32 v139, 0xffc, v138
	v_add_u32_e32 v140, 0x1004, v138
	v_add_u32_e32 v141, 0x103c, v138
	v_add_u32_e32 v142, 0x1044, v138
	ds_read2_b32 v[168:169], v139 offset1:1
	ds_read2_b32 v[170:171], v140 offset1:1
	ds_read2_b32 v[172:173], v141 offset1:1
	ds_read2_b32 v[174:175], v142 offset1:1
	v_add_u32_e32 v139, 0x107c, v138
	v_add_u32_e32 v140, 0x1084, v138
	v_add_u32_e32 v141, 0x10bc, v138
	v_add_u32_e32 v138, 0x10c4, v138
	ds_read2_b32 v[176:177], v139 offset1:1
	ds_read2_b32 v[178:179], v140 offset1:1
	ds_read2_b32 v[180:181], v141 offset1:1
	ds_read2_b32 v[182:183], v138 offset1:1

; __device__ __forceinline__ unsigned xb_add(unsigned* p, unsigned v) { return __hip_atomic_fetch_add(p, v, __ATOMIC_RELAXED, __HIP_MEMORY_SCOPE_AGENT); }
; __device__ __forceinline__ void xcd_barrier(const XcdBarrier& b) {
;     asm volatile("s_waitcnt vmcnt(0)" ::: "memory");
;     __syncthreads();
;     if (threadIdx.x == 0) {
;         unsigned* bar = b.bar;
;         __builtin_amdgcn_s_waitcnt(0);
;         unsigned nloc = b.st[0], nx = b.st[1];
;         if (nloc == 0u) { xcd_barrier_complete(bar, b.x, nloc, nx); b.st[0] = nloc; b.st[1] = nx; }
;         const unsigned old = xb_add(&bar[XB_XSUB(b.x)], 1u);
.LBB0_1311:
	v_readlane_b32 s90, v254, 3
	v_readlane_b32 s91, v254, 4
	v_readlane_b32 s0, v254, 30
	s_add_i32 s16, s0, 7
	v_readlane_b32 s0, v251, 3
	v_readlane_b32 s1, v251, 4
	s_cmp_ge_i32 s16, s1
	s_waitcnt lgkmcnt(0)
	s_barrier
	s_cbranch_scc1 .LBB0_1361
	s_waitcnt vmcnt(0)
	s_barrier
	s_mov_b64 s[0:1], exec
	v_readlane_b32 s2, v253, 41
	v_readlane_b32 s3, v253, 42
	s_and_b64 s[2:3], s[0:1], s[2:3]
	s_mov_b64 exec, s[2:3]
	s_cbranch_execz .LBB0_1360
	v_readlane_b32 s2, v253, 7
	s_waitcnt vmcnt(0) expcnt(0) lgkmcnt(0)
	s_nop 0
	v_mov_b32_e32 v0, s2
	ds_read_b32 v3, v0
	v_readlane_b32 s2, v253, 8
	s_waitcnt lgkmcnt(0)
	v_cmp_ne_u32_e32 vcc, 0, v3
	v_mov_b32_e32 v0, s2
	ds_read_b32 v2, v0
	s_cbranch_vccnz .LBB0_1328
	v_readlane_b32 s4, v251, 1
	v_readlane_b32 s5, v251, 2
	s_load_dwordx2 s[2:3], s[4:5], 0x4
	s_mov_b32 s9, 1
	s_waitcnt lgkmcnt(0)
	s_mul_i32 s8, s2, s74
	s_mul_i32 s8, s8, s3
	s_branch .LBB0_1316
